# write-through (sc1) stores for the MLA and SB attention output tiles (full 128-B lines) in front of the grid barrier
# speedup vs baseline: 1.0088x; 1.0088x over previous
; #define LAS __attribute__((address_space(3)))
; __device__ __forceinline__ unsigned cvt_pk_bf16(float lo, float hi) { unsigned r; asm volatile("v_cvt_pk_bf16_f32 %0, %1, %2" : "=v"(r) : "v"(lo), "v"(hi)); return r; }
; __device__ __forceinline__ float bf_lo(unsigned u) { return __uint_as_float(u << 16); }
; __device__ __forceinline__ float bf_hi(unsigned u) { return __uint_as_float(u & 0xffff0000u); }
; __device__ __forceinline__ int crow(int r, int hi) { return (r & 3) + 8 * (r >> 2) + 4 * hi; }
; __device__ __forceinline__ void store_o(const f32x16 (&o)[2], const float (&sc)[16], bf16_t* Ow, float* ssq  , ldsp stg, int lane, int r32, int hi) {
;     LAS bf16_t* s = (LAS bf16_t*)stg;
; #pragma unroll
;     for (int r = 0; r < 16; ++r) { const int orow = crow(r, hi);
; #pragma unroll
;         for (int d0 = 0; d0 < 2; ++d0) s[orow * 64 + d0 * 32 + r32] = (bf16_t)(cvt_pk_bf16(o[d0][r] * sc[r], 0.f) & 0xffffu); }
;     asm volatile("s_waitcnt lgkmcnt(0)" ::: "memory");
; #pragma unroll
;     for (int i = 0; i < 4; ++i) { const int row = i * 8 + (lane >> 3), ch = lane & 7; const u32x4 v = *(const LAS u32x4*)(s + row * 64 + ch * 8);
;         gst16(Ow + (size_t)row * 1024 + ch * 8, v);
;         float q = 0.f;
; #pragma unroll
;         for (int j = 0; j < 4; ++j) { const float a = bf_lo(v[j]), b = bf_hi(v[j]); q += a * a + b * b; }
;         q += __shfl_xor(q, 1); q += __shfl_xor(q, 2); q += __shfl_xor(q, 4);
;         if (ch == 0) ssq[(size_t)row * 16] = q; }
; }
; __device__ __forceinline__ void sb_unit(int b, int h, int qb, const bf16_t* __restrict__ PROJ, bf16_t* OCAT, float* SSQO, ldsp shm, volatile LAS unsigned* FL) {
;     ...
;     store_o(o, sc, OCAT + row0 * 1024 + 512 + h * 64, SSQO + row0 * 16 + 8 + h, shm + SB_OST + wid * 4096, lane, r32, hi);
.LBB0_1065:
	s_lshl_b64 s[0:1], s[14:15], 11
	s_add_u32 s0, s30, s0
	s_addc_u32 s1, s31, s1
	s_lshl_b32 s2, s22, 1
	s_add_u32 s4, s0, s2
	s_mul_hi_u32 s3, s14, 0xfffff840
	s_addc_u32 s5, s1, 0
	s_mul_i32 s2, s15, 0xfffff840
	s_sub_i32 s3, s3, s14
	s_add_i32 s3, s3, s2
	s_mul_i32 s2, s14, 0xfffff840
	s_add_u32 s0, s0, s2
	s_addc_u32 s1, s1, s3
	s_lshl_b32 s2, s21, 2
	s_add_u32 s0, s0, s2
	s_addc_u32 s1, s1, 0
	s_add_u32 s0, s0, 0x4e4020
	s_addc_u32 s1, s1, 0
	s_lshl_b32 s2, s20, 12
	s_add_i32 s2, s2, 0
	s_add_i32 s2, s2, 0x10000
	v_lshlrev_b32_e32 v1, 9, v161
	v_lshlrev_b32_e32 v2, 1, v160
	s_waitcnt vmcnt(0)
	v_add3_u32 v1, s2, v1, v2
	v_cvt_pk_bf16_f32 v2, v20, v3
	ds_write_b16 v1, v2
	v_cvt_pk_bf16_f32 v2, v4, v3
	ds_write_b16 v1, v2 offset:64
	v_cvt_pk_bf16_f32 v2, v21, v3
	ds_write_b16 v1, v2 offset:128
	v_cvt_pk_bf16_f32 v2, v5, v3
	ds_write_b16 v1, v2 offset:192
	v_cvt_pk_bf16_f32 v2, v22, v3
	ds_write_b16 v1, v2 offset:256
	v_cvt_pk_bf16_f32 v2, v6, v3
	ds_write_b16 v1, v2 offset:320
	v_cvt_pk_bf16_f32 v2, v23, v3
	ds_write_b16 v1, v2 offset:384
	v_cvt_pk_bf16_f32 v2, v7, v3
	ds_write_b16 v1, v2 offset:448
	v_cvt_pk_bf16_f32 v2, v24, v3
	ds_write_b16 v1, v2 offset:1024
	v_cvt_pk_bf16_f32 v2, v8, v3
	ds_write_b16 v1, v2 offset:1088
	v_cvt_pk_bf16_f32 v2, v25, v3
	ds_write_b16 v1, v2 offset:1152
	v_cvt_pk_bf16_f32 v2, v9, v3
	ds_write_b16 v1, v2 offset:1216
	v_cvt_pk_bf16_f32 v2, v26, v3
	ds_write_b16 v1, v2 offset:1280
	v_cvt_pk_bf16_f32 v2, v10, v3
	ds_write_b16 v1, v2 offset:1344
	v_cvt_pk_bf16_f32 v2, v27, v3
	ds_write_b16 v1, v2 offset:1408
	v_cvt_pk_bf16_f32 v2, v11, v3
	ds_write_b16 v1, v2 offset:1472
	v_cvt_pk_bf16_f32 v2, v28, v3
	ds_write_b16 v1, v2 offset:2048
	v_cvt_pk_bf16_f32 v2, v12, v3
	ds_write_b16 v1, v2 offset:2112
	v_cvt_pk_bf16_f32 v2, v29, v3
	ds_write_b16 v1, v2 offset:2176
	v_cvt_pk_bf16_f32 v2, v13, v3
	ds_write_b16 v1, v2 offset:2240
	v_cvt_pk_bf16_f32 v2, v30, v3
	ds_write_b16 v1, v2 offset:2304
	v_cvt_pk_bf16_f32 v2, v14, v3
	ds_write_b16 v1, v2 offset:2368
	v_cvt_pk_bf16_f32 v2, v31, v3
	ds_write_b16 v1, v2 offset:2432
	v_cvt_pk_bf16_f32 v2, v15, v3
	ds_write_b16 v1, v2 offset:2496
	v_cvt_pk_bf16_f32 v2, v32, v3
	ds_write_b16 v1, v2 offset:3072
	v_cvt_pk_bf16_f32 v2, v16, v3
	ds_write_b16 v1, v2 offset:3136
	v_cvt_pk_bf16_f32 v2, v33, v3
	ds_write_b16 v1, v2 offset:3200
	v_cvt_pk_bf16_f32 v2, v17, v3
	ds_write_b16 v1, v2 offset:3264
	v_cvt_pk_bf16_f32 v2, v34, v3
	ds_write_b16 v1, v2 offset:3328
	v_cvt_pk_bf16_f32 v2, v18, v3
	ds_write_b16 v1, v2 offset:3392
	v_cvt_pk_bf16_f32 v2, v35, v3
	ds_write_b16 v1, v2 offset:3456
	v_cvt_pk_bf16_f32 v2, v19, v3
	v_and_b32_e32 v16, 7, v158
	ds_write_b16 v1, v2 offset:3520
	v_lshlrev_b32_e32 v2, 4, v16
	v_lshrrev_b32_e32 v6, 3, v159
	v_add_u32_e32 v8, s2, v2
	s_waitcnt lgkmcnt(0)
	v_lshl_add_u32 v7, v6, 7, v8
	ds_read_b128 v[12:15], v7
	v_lshl_add_u64 v[4:5], s[4:5], 0, v[2:3]
	v_and_b32_e32 v2, 64, v244
	v_xor_b32_e32 v1, 1, v244
	v_add_u32_e32 v2, 64, v2
	s_waitcnt lgkmcnt(0)
	v_and_b32_e32 v9, 0xffff0000, v12
	v_lshlrev_b32_e32 v7, 16, v12
	v_mul_f32_e32 v9, v9, v9
	v_and_b32_e32 v10, 0xffff0000, v13
	v_fmac_f32_e32 v9, v7, v7
	v_lshlrev_b32_e32 v7, 16, v13
	v_mul_f32_e32 v10, v10, v10
	v_fmac_f32_e32 v10, v7, v7
	v_add_f32_e32 v7, v9, v10
	v_and_b32_e32 v10, 0xffff0000, v14
	v_lshlrev_b32_e32 v9, 16, v14
	v_mul_f32_e32 v10, v10, v10
	v_fmac_f32_e32 v10, v9, v9
	v_add_f32_e32 v7, v10, v7
	v_and_b32_e32 v10, 0xffff0000, v15
	v_cmp_lt_i32_e32 vcc, v1, v2
	v_lshlrev_b32_e32 v9, 16, v15
	v_mul_f32_e32 v10, v10, v10
	v_cndmask_b32_e32 v1, v244, v1, vcc
	v_fmac_f32_e32 v10, v9, v9
	v_lshlrev_b32_e32 v1, 2, v1
	v_add_f32_e32 v9, v10, v7
	ds_bpermute_b32 v10, v1, v9
	v_xor_b32_e32 v7, 2, v244
	v_cmp_lt_i32_e32 vcc, v7, v2
	s_mov_b64 s[2:3], 0x2c8f4400
	v_lshl_add_u64 v[4:5], v[4:5], 0, s[2:3]
	v_cndmask_b32_e32 v7, v244, v7, vcc
	v_lshlrev_b32_e32 v7, 2, v7
	s_waitcnt lgkmcnt(0)
	v_add_f32_e32 v10, v9, v10
	ds_bpermute_b32 v11, v7, v10
	v_xor_b32_e32 v9, 4, v244
	v_cmp_lt_i32_e32 vcc, v9, v2
	s_waitcnt lgkmcnt(0)
	v_add_f32_e32 v10, v10, v11
	v_cndmask_b32_e32 v2, v244, v9, vcc
	v_lshlrev_b32_e32 v9, 2, v2
	ds_bpermute_b32 v11, v9, v10
	v_lshlrev_b32_e32 v2, 11, v6
	v_cmp_eq_u32_e32 vcc, 0, v16
	v_lshl_add_u64 v[16:17], v[4:5], 0, v[2:3]
	global_store_dwordx4 v[16:17], v[12:15], off sc1
	s_and_saveexec_b64 s[4:5], vcc
	s_cbranch_execz .LBB0_1067
	v_lshlrev_b32_e32 v2, 6, v6
	v_lshl_add_u64 v[12:13], s[0:1], 0, v[2:3]
	s_waitcnt lgkmcnt(0)
	v_add_f32_e32 v2, v10, v11
	flat_store_dword v[12:13], v2 sc1
; #define LAS __attribute__((address_space(3)))
; __device__ __forceinline__ float bf_lo(unsigned u) { return __uint_as_float(u << 16); }
; __device__ __forceinline__ float bf_hi(unsigned u) { return __uint_as_float(u & 0xffff0000u); }
; __device__ __forceinline__ void store_o(const f32x16 (&o)[2], const float (&sc)[16], bf16_t* Ow, float* ssq  , ldsp stg, int lane, int r32, int hi) {
;     ...
;     for (int i = 0; i < 4; ++i) { const int row = i * 8 + (lane >> 3), ch = lane & 7; const u32x4 v = *(const LAS u32x4*)(s + row * 64 + ch * 8);
;         gst16(Ow + (size_t)row * 1024 + ch * 8, v);
;         float q = 0.f;
; #pragma unroll
;         for (int j = 0; j < 4; ++j) { const float a = bf_lo(v[j]), b = bf_hi(v[j]); q += a * a + b * b; }
;         q += __shfl_xor(q, 1); q += __shfl_xor(q, 2); q += __shfl_xor(q, 4);
;         if (ch == 0) ssq[(size_t)row * 16] = q; }
; }
.LBB0_1067:
	s_or_b64 exec, exec, s[4:5]
	v_or_b32_e32 v10, 8, v6
	v_lshl_add_u32 v2, v10, 7, v8
	ds_read_b128 v[12:15], v2
	v_lshlrev_b32_e32 v2, 11, v10
	v_lshl_add_u64 v[16:17], v[4:5], 0, v[2:3]
	s_waitcnt lgkmcnt(0)
	v_and_b32_e32 v11, 0xffff0000, v12
	global_store_dwordx4 v[16:17], v[12:15], off sc1
	v_lshlrev_b32_e32 v2, 16, v12
	v_mul_f32_e32 v11, v11, v11
	v_and_b32_e32 v12, 0xffff0000, v13
	v_fmac_f32_e32 v11, v2, v2
	v_lshlrev_b32_e32 v2, 16, v13
	v_mul_f32_e32 v12, v12, v12
	v_fmac_f32_e32 v12, v2, v2
	v_add_f32_e32 v2, v11, v12
	v_and_b32_e32 v12, 0xffff0000, v14
	v_lshlrev_b32_e32 v11, 16, v14
	v_mul_f32_e32 v12, v12, v12
	v_fmac_f32_e32 v12, v11, v11
	v_add_f32_e32 v2, v12, v2
	v_and_b32_e32 v12, 0xffff0000, v15
	v_lshlrev_b32_e32 v11, 16, v15
	v_mul_f32_e32 v12, v12, v12
	v_fmac_f32_e32 v12, v11, v11
	v_add_f32_e32 v2, v12, v2
	ds_bpermute_b32 v11, v1, v2
	s_waitcnt lgkmcnt(0)
	v_add_f32_e32 v2, v2, v11
	ds_bpermute_b32 v11, v7, v2
	s_waitcnt lgkmcnt(0)
	v_add_f32_e32 v11, v2, v11
	ds_bpermute_b32 v12, v9, v11
	s_and_saveexec_b64 s[4:5], vcc
	s_cbranch_execz .LBB0_1069
	v_lshlrev_b32_e32 v2, 6, v10
	v_lshl_add_u64 v[14:15], s[0:1], 0, v[2:3]
	s_waitcnt lgkmcnt(0)
	v_add_f32_e32 v2, v11, v12
	flat_store_dword v[14:15], v2 sc1
.LBB0_1069:
	s_or_b64 exec, exec, s[4:5]
	v_or_b32_e32 v10, 16, v6
	v_lshl_add_u32 v2, v10, 7, v8
	s_waitcnt lgkmcnt(0)
	ds_read_b128 v[12:15], v2
	v_lshlrev_b32_e32 v2, 11, v10
	v_lshl_add_u64 v[16:17], v[4:5], 0, v[2:3]
	s_waitcnt lgkmcnt(0)
	v_and_b32_e32 v11, 0xffff0000, v12
	global_store_dwordx4 v[16:17], v[12:15], off sc1
	v_lshlrev_b32_e32 v2, 16, v12
	v_mul_f32_e32 v11, v11, v11
	v_and_b32_e32 v12, 0xffff0000, v13
	v_fmac_f32_e32 v11, v2, v2
	v_lshlrev_b32_e32 v2, 16, v13
	v_mul_f32_e32 v12, v12, v12
	v_fmac_f32_e32 v12, v2, v2
	v_add_f32_e32 v2, v11, v12
	v_and_b32_e32 v12, 0xffff0000, v14
	v_lshlrev_b32_e32 v11, 16, v14
	v_mul_f32_e32 v12, v12, v12
	v_fmac_f32_e32 v12, v11, v11
	v_add_f32_e32 v2, v12, v2
	v_and_b32_e32 v12, 0xffff0000, v15
	v_lshlrev_b32_e32 v11, 16, v15
	v_mul_f32_e32 v12, v12, v12
	v_fmac_f32_e32 v12, v11, v11
	v_add_f32_e32 v2, v12, v2
	ds_bpermute_b32 v11, v1, v2
	s_waitcnt lgkmcnt(0)
	v_add_f32_e32 v2, v2, v11
	ds_bpermute_b32 v11, v7, v2
	s_waitcnt lgkmcnt(0)
	v_add_f32_e32 v11, v2, v11
	ds_bpermute_b32 v12, v9, v11
	s_and_saveexec_b64 s[4:5], vcc
	s_cbranch_execz .LBB0_1071
	v_lshlrev_b32_e32 v2, 6, v10
	v_lshl_add_u64 v[14:15], s[0:1], 0, v[2:3]
	s_waitcnt lgkmcnt(0)
	v_add_f32_e32 v2, v11, v12
	flat_store_dword v[14:15], v2 sc1
.LBB0_1071:
	s_or_b64 exec, exec, s[4:5]
	v_or_b32_e32 v6, 24, v6
	v_lshl_add_u32 v2, v6, 7, v8
	s_waitcnt lgkmcnt(0)
	ds_read_b128 v[10:13], v2
	v_lshlrev_b32_e32 v2, 11, v6
	v_lshl_add_u64 v[4:5], v[4:5], 0, v[2:3]
	s_waitcnt lgkmcnt(0)
	global_store_dwordx4 v[4:5], v[10:13], off sc1
	v_and_b32_e32 v4, 0xffff0000, v10
	v_lshlrev_b32_e32 v2, 16, v10
	v_mul_f32_e32 v4, v4, v4
	v_and_b32_e32 v5, 0xffff0000, v11
	v_fmac_f32_e32 v4, v2, v2
	v_lshlrev_b32_e32 v2, 16, v11
	v_mul_f32_e32 v5, v5, v5
	v_fmac_f32_e32 v5, v2, v2
	v_add_f32_e32 v2, v4, v5
	v_and_b32_e32 v5, 0xffff0000, v12
	v_lshlrev_b32_e32 v4, 16, v12
	v_mul_f32_e32 v5, v5, v5
	v_fmac_f32_e32 v5, v4, v4
	v_add_f32_e32 v2, v5, v2
	v_and_b32_e32 v5, 0xffff0000, v13
	v_lshlrev_b32_e32 v4, 16, v13
	v_mul_f32_e32 v5, v5, v5
	v_fmac_f32_e32 v5, v4, v4
	v_add_f32_e32 v2, v5, v2
	ds_bpermute_b32 v1, v1, v2
	s_waitcnt lgkmcnt(0)
	v_add_f32_e32 v1, v2, v1
	ds_bpermute_b32 v2, v7, v1
	s_waitcnt lgkmcnt(0)
	v_add_f32_e32 v1, v1, v2
	ds_bpermute_b32 v4, v9, v1
	s_and_saveexec_b64 s[4:5], vcc
	s_cbranch_execz .LBB0_1045
	v_lshlrev_b32_e32 v2, 6, v6
	v_lshl_add_u64 v[6:7], s[0:1], 0, v[2:3]
	s_waitcnt lgkmcnt(0)
	v_add_f32_e32 v1, v1, v4
	flat_store_dword v[6:7], v1 sc1
	s_branch .LBB0_1045

; #define LAS __attribute__((address_space(3)))
; __device__ __forceinline__ unsigned cvt_pk_bf16(float lo, float hi) { unsigned r; asm volatile("v_cvt_pk_bf16_f32 %0, %1, %2" : "=v"(r) : "v"(lo), "v"(hi)); return r; }
; __device__ __forceinline__ float rcpf_(float x) { return __builtin_amdgcn_rcpf(x); }
; __device__ __forceinline__ int crow(int r, int hi) { return (r & 3) + 8 * (r >> 2) + 4 * hi; }
; #define ATT_WAITBAR() asm volatile("s_waitcnt vmcnt(0) lgkmcnt(0)\n\ts_barrier" ::: "memory")
; __device__ __forceinline__ float swapsum(float m) { auto rr = __builtin_amdgcn_permlane32_swap(__float_as_uint(m), __float_as_uint(m), false, false); return __uint_as_float(rr[0]) + __uint_as_float(rr[1]); }
; __device__ __forceinline__ u32x4 packp(const f32x16& p, int b) { u32x4 w; w.x = cvt_pk_bf16(p[b], p[b + 1]); w.y = cvt_pk_bf16(p[b + 2], p[b + 3]); w.z = cvt_pk_bf16(p[b + 4], p[b + 5]); w.w = cvt_pk_bf16(p[b + 6], p[b + 7]); return w; }
; __device__ __forceinline__ void store_o(const f32x16 (&o)[2], const float (&sc)[16], bf16_t* Ow, float* ssq  , ldsp stg, int lane, int r32, int hi) {
;     LAS bf16_t* s = (LAS bf16_t*)stg;
; #pragma unroll
;     for (int r = 0; r < 16; ++r) { const int orow = crow(r, hi);
; #pragma unroll
;         for (int d0 = 0; d0 < 2; ++d0) s[orow * 64 + d0 * 32 + r32] = (bf16_t)(cvt_pk_bf16(o[d0][r] * sc[r], 0.f) & 0xffffu); }
; __device__ __forceinline__ void mla_unit(int b, int h, int qb, const bf16_t* __restrict__ Q, const bf16_t* __restrict__ KV, const bf16_t* __restrict__ PROJ, bf16_t* OCAT, float* SSQO, ldsp shm) {
;     ...
;     { float sacc = 0.f;
; #pragma unroll
;       for (int r = 0; r < 16; ++r) sacc += pB0[r] + pB1[r];
;       l_reg += sacc;
;       ATT_WAITBAR();
;       pv(o, vp0 + ((NT - 1) & 3) * VS, packp(pB0, 0), packp(pB0, 8), packp(pB1, 0), packp(pB1, 8)); }
;     ...
;     l_reg = swapsum(l_reg);
;     if (hi == 0) wsf[32 + r32] = l_reg;
;     asm volatile("s_waitcnt lgkmcnt(0)" ::: "memory");
;     float sc[16];
; #pragma unroll
;     for (int r = 0; r < 16; ++r) sc[r] = rcpf_(wsf[32 + crow(r, hi)]);
;     const size_t row0 = rowbase + q0 + wid * 32;
;     store_o(o, sc, OCAT + row0 * 1024 + h * 64, SSQO + row0 * 16 + h, shm + OST_OFF + wid * 4096, lane, r32, hi);
.LBB0_1185:
	v_add_f32_e32 v52, v84, v36
	v_add_f32_e32 v52, 0, v52
	v_add_f32_e32 v54, v85, v37
	v_add_f32_e32 v52, v54, v52
	v_add_f32_e32 v54, v86, v38
	v_add_f32_e32 v52, v54, v52
	v_add_f32_e32 v54, v87, v39
	v_add_f32_e32 v52, v54, v52
	v_add_f32_e32 v54, v88, v40
	v_add_f32_e32 v52, v54, v52
	v_add_f32_e32 v54, v89, v41
	v_add_f32_e32 v52, v54, v52
	v_add_f32_e32 v54, v90, v42
	v_add_f32_e32 v52, v54, v52
	v_add_f32_e32 v54, v91, v43
	v_add_f32_e32 v52, v54, v52
	v_add_f32_e32 v54, v92, v44
	v_add_f32_e32 v52, v54, v52
	v_add_f32_e32 v54, v93, v45
	v_add_f32_e32 v52, v54, v52
	v_add_f32_e32 v54, v94, v46
	v_add_f32_e32 v52, v54, v52
	v_add_f32_e32 v54, v95, v47
	v_add_f32_e32 v52, v54, v52
	v_add_f32_e32 v54, v96, v48
	v_add_f32_e32 v52, v54, v52
	v_add_f32_e32 v54, v97, v49
	v_add_f32_e32 v52, v54, v52
	v_add_f32_e32 v54, v98, v50
	v_add_u32_e32 v53, 0xc000, v186
	v_add_f32_e32 v52, v54, v52
	v_add_f32_e32 v54, v99, v51
	v_add_f32_e32 v52, v54, v52
	s_waitcnt vmcnt(0) lgkmcnt(0)
	s_barrier
	v_cvt_pk_bf16_f32 v54, v84, v85
	v_cvt_pk_bf16_f32 v55, v86, v87
	v_cvt_pk_bf16_f32 v56, v88, v89
	v_cvt_pk_bf16_f32 v57, v90, v91
	v_cvt_pk_bf16_f32 v58, v92, v93
	v_cvt_pk_bf16_f32 v59, v94, v95
	v_cvt_pk_bf16_f32 v60, v96, v97
	v_cvt_pk_bf16_f32 v61, v98, v99
	v_cvt_pk_bf16_f32 v62, v36, v37
	v_cvt_pk_bf16_f32 v63, v38, v39
	v_cvt_pk_bf16_f32 v64, v40, v41
	v_cvt_pk_bf16_f32 v65, v42, v43
	v_cvt_pk_bf16_f32 v36, v44, v45
	v_cvt_pk_bf16_f32 v37, v46, v47
	v_cvt_pk_bf16_f32 v38, v48, v49
	v_cvt_pk_bf16_f32 v39, v50, v51
	ds_read_b64_tr_b16 v[40:41], v53 offset:24576
	ds_read_b64_tr_b16 v[42:43], v53 offset:25088
	ds_read_b64_tr_b16 v[44:45], v53 offset:25600
	ds_read_b64_tr_b16 v[46:47], v53 offset:26112
	ds_read_b64_tr_b16 v[48:49], v53 offset:26624
	ds_read_b64_tr_b16 v[50:51], v53 offset:27136
	ds_read_b64_tr_b16 v[66:67], v53 offset:27648
	ds_read_b64_tr_b16 v[68:69], v53 offset:28160
	s_waitcnt lgkmcnt(0)
	v_mfma_f32_32x32x16_bf16 v[4:19], v[54:57], v[40:43], v[4:19]
	v_add_f32_e32 v52, v116, v52
	v_mfma_f32_32x32x16_bf16 v[4:19], v[58:61], v[44:47], v[4:19]
	v_mfma_f32_32x32x16_bf16 v[4:19], v[62:65], v[48:51], v[4:19]
	v_mfma_f32_32x32x16_bf16 v[4:19], v[36:39], v[66:69], v[4:19]
	ds_read_b64_tr_b16 v[40:41], v53 offset:28672
	ds_read_b64_tr_b16 v[42:43], v53 offset:29184
	ds_read_b64_tr_b16 v[44:45], v53 offset:29696
	ds_read_b64_tr_b16 v[46:47], v53 offset:30208
	ds_read_b64_tr_b16 v[48:49], v53 offset:30720
	ds_read_b64_tr_b16 v[50:51], v53 offset:31232
	ds_read_b64_tr_b16 v[66:67], v53 offset:31744
	ds_read_b64_tr_b16 v[68:69], v53 offset:32256
	s_waitcnt lgkmcnt(0)
	v_mfma_f32_32x32x16_bf16 v[20:35], v[54:57], v[40:43], v[20:35]
	v_mfma_f32_32x32x16_bf16 v[20:35], v[58:61], v[44:47], v[20:35]
	v_mfma_f32_32x32x16_bf16 v[20:35], v[62:65], v[48:51], v[20:35]
	v_mfma_f32_32x32x16_bf16 v[20:35], v[36:39], v[66:69], v[20:35]
	v_mov_b32_e32 v36, v52
	s_nop 1
	v_permlane32_swap_b32_e32 v52, v36
	s_and_saveexec_b64 s[10:11], s[36:37]
	v_add_f32_e32 v36, v52, v36
	ds_write_b32 v185, v36 offset:128
	s_or_b64 exec, exec, s[10:11]
	s_waitcnt lgkmcnt(0)
	ds_read_b128 v[36:39], v2 offset:128
	ds_read_b128 v[40:43], v2 offset:160
	s_lshl_b64 s[2:3], s[30:31], 11
	s_add_u32 s2, s42, s2
	s_addc_u32 s3, s43, s3
	s_lshl_b32 s8, s49, 7
	s_add_u32 s12, s2, s8
	s_addc_u32 s13, s3, 0
	s_lshl_b64 s[2:3], s[30:31], 6
	s_waitcnt lgkmcnt(0)
	v_rcp_f32_e32 v44, v36
	v_rcp_f32_e32 v45, v37
	v_rcp_f32_e32 v46, v38
	v_rcp_f32_e32 v47, v39
	v_rcp_f32_e32 v48, v40
	ds_read_b128 v[36:39], v2 offset:192
	v_rcp_f32_e32 v49, v41
	v_rcp_f32_e32 v50, v42
	v_rcp_f32_e32 v51, v43
	ds_read_b128 v[40:43], v2 offset:224
	s_add_u32 s2, s44, s2
	s_addc_u32 s3, s45, s3
	s_lshl_b32 s8, s49, 2
	s_add_u32 s10, s2, s8
	s_addc_u32 s11, s3, 0
	s_lshl_b32 s2, s50, 12
	s_add_i32 s2, s2, 0
	s_waitcnt lgkmcnt(0)
	v_rcp_f32_e32 v2, v36
	v_rcp_f32_e32 v36, v37
	v_rcp_f32_e32 v37, v38
	v_rcp_f32_e32 v38, v39
	v_rcp_f32_e32 v39, v40
	v_rcp_f32_e32 v40, v41
	v_rcp_f32_e32 v41, v42
	v_rcp_f32_e32 v42, v43
	s_add_i32 s2, s2, 0x14800
	v_lshlrev_b32_e32 v43, 9, v184
	v_lshlrev_b32_e32 v52, 1, v183
	v_mul_f32_e32 v4, v4, v44
	v_add3_u32 v43, s2, v43, v52
	v_cvt_pk_bf16_f32 v4, v4, v3
	ds_write_b16 v43, v4
	v_mul_f32_e32 v4, v20, v44
	v_cvt_pk_bf16_f32 v4, v4, v3
	ds_write_b16 v43, v4 offset:64
	v_mul_f32_e32 v4, v5, v45
	v_cvt_pk_bf16_f32 v4, v4, v3
	ds_write_b16 v43, v4 offset:128
	v_mul_f32_e32 v4, v21, v45
	v_cvt_pk_bf16_f32 v4, v4, v3
	ds_write_b16 v43, v4 offset:192
	v_mul_f32_e32 v4, v6, v46
	v_cvt_pk_bf16_f32 v4, v4, v3
	ds_write_b16 v43, v4 offset:256
	v_mul_f32_e32 v4, v22, v46
	v_cvt_pk_bf16_f32 v4, v4, v3
	ds_write_b16 v43, v4 offset:320
	v_mul_f32_e32 v4, v7, v47
	v_cvt_pk_bf16_f32 v4, v4, v3
	ds_write_b16 v43, v4 offset:384
	v_mul_f32_e32 v4, v23, v47
	v_cvt_pk_bf16_f32 v4, v4, v3
	ds_write_b16 v43, v4 offset:448
	v_mul_f32_e32 v4, v8, v48
	v_cvt_pk_bf16_f32 v4, v4, v3
	ds_write_b16 v43, v4 offset:1024
	v_mul_f32_e32 v4, v24, v48
	v_cvt_pk_bf16_f32 v4, v4, v3
	ds_write_b16 v43, v4 offset:1088
	v_mul_f32_e32 v4, v9, v49
	v_cvt_pk_bf16_f32 v4, v4, v3
	ds_write_b16 v43, v4 offset:1152
	v_mul_f32_e32 v4, v25, v49
	v_cvt_pk_bf16_f32 v4, v4, v3
	ds_write_b16 v43, v4 offset:1216
	v_mul_f32_e32 v4, v10, v50
	v_cvt_pk_bf16_f32 v4, v4, v3
	ds_write_b16 v43, v4 offset:1280
	v_mul_f32_e32 v4, v26, v50
	v_cvt_pk_bf16_f32 v4, v4, v3
	ds_write_b16 v43, v4 offset:1344
	v_mul_f32_e32 v4, v11, v51
	v_cvt_pk_bf16_f32 v4, v4, v3
	ds_write_b16 v43, v4 offset:1408
	v_mul_f32_e32 v4, v27, v51
	v_cvt_pk_bf16_f32 v4, v4, v3
	ds_write_b16 v43, v4 offset:1472
	v_mul_f32_e32 v4, v12, v2
	v_mul_f32_e32 v2, v28, v2
; #define LAS __attribute__((address_space(3)))
; __device__ __forceinline__ unsigned cvt_pk_bf16(float lo, float hi) { unsigned r; asm volatile("v_cvt_pk_bf16_f32 %0, %1, %2" : "=v"(r) : "v"(lo), "v"(hi)); return r; }
; __device__ __forceinline__ float bf_lo(unsigned u) { return __uint_as_float(u << 16); }
; __device__ __forceinline__ float bf_hi(unsigned u) { return __uint_as_float(u & 0xffff0000u); }
; __device__ __forceinline__ int crow(int r, int hi) { return (r & 3) + 8 * (r >> 2) + 4 * hi; }
; __device__ __forceinline__ void store_o(const f32x16 (&o)[2], const float (&sc)[16], bf16_t* Ow, float* ssq  , ldsp stg, int lane, int r32, int hi) {
;     LAS bf16_t* s = (LAS bf16_t*)stg;
; #pragma unroll
;     for (int r = 0; r < 16; ++r) { const int orow = crow(r, hi);
; #pragma unroll
;         for (int d0 = 0; d0 < 2; ++d0) s[orow * 64 + d0 * 32 + r32] = (bf16_t)(cvt_pk_bf16(o[d0][r] * sc[r], 0.f) & 0xffffu); }
;     asm volatile("s_waitcnt lgkmcnt(0)" ::: "memory");
; #pragma unroll
;     for (int i = 0; i < 4; ++i) { const int row = i * 8 + (lane >> 3), ch = lane & 7; const u32x4 v = *(const LAS u32x4*)(s + row * 64 + ch * 8);
;         gst16(Ow + (size_t)row * 1024 + ch * 8, v);
;         float q = 0.f;
; #pragma unroll
;         for (int j = 0; j < 4; ++j) { const float a = bf_lo(v[j]), b = bf_hi(v[j]); q += a * a + b * b; }
;         q += __shfl_xor(q, 1); q += __shfl_xor(q, 2); q += __shfl_xor(q, 4);
;         if (ch == 0) ssq[(size_t)row * 16] = q; }
	v_cvt_pk_bf16_f32 v4, v4, v3
	ds_write_b16 v43, v4 offset:2048
	v_cvt_pk_bf16_f32 v2, v2, v3
	ds_write_b16 v43, v2 offset:2112
	v_mul_f32_e32 v2, v13, v36
	v_cvt_pk_bf16_f32 v2, v2, v3
	ds_write_b16 v43, v2 offset:2176
	v_mul_f32_e32 v2, v29, v36
	v_cvt_pk_bf16_f32 v2, v2, v3
	ds_write_b16 v43, v2 offset:2240
	v_mul_f32_e32 v2, v14, v37
	v_cvt_pk_bf16_f32 v2, v2, v3
	ds_write_b16 v43, v2 offset:2304
	v_mul_f32_e32 v2, v30, v37
	v_cvt_pk_bf16_f32 v2, v2, v3
	ds_write_b16 v43, v2 offset:2368
	v_mul_f32_e32 v2, v15, v38
	v_cvt_pk_bf16_f32 v2, v2, v3
	ds_write_b16 v43, v2 offset:2432
	v_mul_f32_e32 v2, v31, v38
	v_cvt_pk_bf16_f32 v2, v2, v3
	ds_write_b16 v43, v2 offset:2496
	v_mul_f32_e32 v2, v16, v39
	v_cvt_pk_bf16_f32 v2, v2, v3
	ds_write_b16 v43, v2 offset:3072
	v_mul_f32_e32 v2, v32, v39
	v_cvt_pk_bf16_f32 v2, v2, v3
	ds_write_b16 v43, v2 offset:3136
	v_mul_f32_e32 v2, v17, v40
	v_cvt_pk_bf16_f32 v2, v2, v3
	ds_write_b16 v43, v2 offset:3200
	v_mul_f32_e32 v2, v33, v40
	v_cvt_pk_bf16_f32 v2, v2, v3
	ds_write_b16 v43, v2 offset:3264
	v_mul_f32_e32 v2, v18, v41
	v_cvt_pk_bf16_f32 v2, v2, v3
	ds_write_b16 v43, v2 offset:3328
	v_mul_f32_e32 v2, v34, v41
	v_cvt_pk_bf16_f32 v2, v2, v3
	ds_write_b16 v43, v2 offset:3392
	v_mul_f32_e32 v2, v19, v42
	v_cvt_pk_bf16_f32 v2, v2, v3
	ds_write_b16 v43, v2 offset:3456
	v_mul_f32_e32 v2, v35, v42
	v_cvt_pk_bf16_f32 v2, v2, v3
	v_and_b32_e32 v16, 7, v1
	ds_write_b16 v43, v2 offset:3520
	v_lshlrev_b32_e32 v2, 4, v16
	v_lshrrev_b32_e32 v7, 3, v182
	v_add_u32_e32 v8, s2, v2
	s_waitcnt lgkmcnt(0)
	v_lshl_add_u32 v6, v7, 7, v8
	ds_read_b128 v[12:15], v6
	v_lshl_add_u64 v[4:5], s[12:13], 0, v[2:3]
	v_and_b32_e32 v2, 64, v244
	v_xor_b32_e32 v1, 1, v244
	v_add_u32_e32 v2, 64, v2
	s_waitcnt lgkmcnt(0)
	v_and_b32_e32 v9, 0xffff0000, v12
	v_lshlrev_b32_e32 v6, 16, v12
	v_mul_f32_e32 v9, v9, v9
	v_and_b32_e32 v10, 0xffff0000, v13
	v_fmac_f32_e32 v9, v6, v6
	v_lshlrev_b32_e32 v6, 16, v13
	v_mul_f32_e32 v10, v10, v10
	v_fmac_f32_e32 v10, v6, v6
	v_add_f32_e32 v6, v9, v10
	v_and_b32_e32 v10, 0xffff0000, v14
	v_lshlrev_b32_e32 v9, 16, v14
	v_mul_f32_e32 v10, v10, v10
	v_fmac_f32_e32 v10, v9, v9
	v_add_f32_e32 v6, v10, v6
	v_and_b32_e32 v10, 0xffff0000, v15
	v_cmp_lt_i32_e32 vcc, v1, v2
	v_lshlrev_b32_e32 v9, 16, v15
	v_mul_f32_e32 v10, v10, v10
	v_cndmask_b32_e32 v1, v244, v1, vcc
	v_fmac_f32_e32 v10, v9, v9
	v_lshlrev_b32_e32 v1, 2, v1
	v_add_f32_e32 v9, v10, v6
	ds_bpermute_b32 v10, v1, v9
	v_xor_b32_e32 v6, 2, v244
	v_cmp_lt_i32_e32 vcc, v6, v2
	s_waitcnt lgkmcnt(0)
	v_add_f32_e32 v10, v9, v10
	v_cndmask_b32_e32 v6, v244, v6, vcc
	v_lshlrev_b32_e32 v6, 2, v6
	ds_bpermute_b32 v11, v6, v10
	v_xor_b32_e32 v9, 4, v244
	v_cmp_lt_i32_e32 vcc, v9, v2
	s_waitcnt lgkmcnt(0)
	v_add_f32_e32 v10, v10, v11
	v_cndmask_b32_e32 v2, v244, v9, vcc
	v_lshlrev_b32_e32 v9, 2, v2
	ds_bpermute_b32 v11, v9, v10
	v_lshlrev_b32_e32 v2, 11, v7
	v_cmp_eq_u32_e32 vcc, 0, v16
	v_lshl_add_u64 v[16:17], v[4:5], 0, v[2:3]
	global_store_dwordx4 v[16:17], v[12:15], off sc1
	s_and_saveexec_b64 s[12:13], vcc
	v_readlane_b32 s26, v255, 34
	v_readlane_b32 s27, v255, 35
	s_cbranch_execz .LBB0_1189
	v_lshlrev_b32_e32 v2, 6, v7
	v_lshl_add_u64 v[12:13], s[10:11], 0, v[2:3]
	s_waitcnt lgkmcnt(0)
	v_add_f32_e32 v2, v10, v11
	flat_store_dword v[12:13], v2 sc1
; #define LAS __attribute__((address_space(3)))
; __device__ __forceinline__ float bf_lo(unsigned u) { return __uint_as_float(u << 16); }
; __device__ __forceinline__ float bf_hi(unsigned u) { return __uint_as_float(u & 0xffff0000u); }
; __device__ __forceinline__ void store_o(const f32x16 (&o)[2], const float (&sc)[16], bf16_t* Ow, float* ssq  , ldsp stg, int lane, int r32, int hi) {
;     ...
;     for (int i = 0; i < 4; ++i) { const int row = i * 8 + (lane >> 3), ch = lane & 7; const u32x4 v = *(const LAS u32x4*)(s + row * 64 + ch * 8);
;         gst16(Ow + (size_t)row * 1024 + ch * 8, v);
;         float q = 0.f;
; #pragma unroll
;         for (int j = 0; j < 4; ++j) { const float a = bf_lo(v[j]), b = bf_hi(v[j]); q += a * a + b * b; }
;         q += __shfl_xor(q, 1); q += __shfl_xor(q, 2); q += __shfl_xor(q, 4);
;         if (ch == 0) ssq[(size_t)row * 16] = q; }
.LBB0_1189:
	s_or_b64 exec, exec, s[12:13]
	v_or_b32_e32 v10, 8, v7
	v_lshl_add_u32 v2, v10, 7, v8
	ds_read_b128 v[12:15], v2
	v_lshlrev_b32_e32 v2, 11, v10
	v_lshl_add_u64 v[16:17], v[4:5], 0, v[2:3]
	s_waitcnt lgkmcnt(0)
	v_and_b32_e32 v11, 0xffff0000, v12
	global_store_dwordx4 v[16:17], v[12:15], off sc1
	v_lshlrev_b32_e32 v2, 16, v12
	v_mul_f32_e32 v11, v11, v11
	v_and_b32_e32 v12, 0xffff0000, v13
	v_fmac_f32_e32 v11, v2, v2
	v_lshlrev_b32_e32 v2, 16, v13
	v_mul_f32_e32 v12, v12, v12
	v_fmac_f32_e32 v12, v2, v2
	v_add_f32_e32 v2, v11, v12
	v_and_b32_e32 v12, 0xffff0000, v14
	v_lshlrev_b32_e32 v11, 16, v14
	v_mul_f32_e32 v12, v12, v12
	v_fmac_f32_e32 v12, v11, v11
	v_add_f32_e32 v2, v12, v2
	v_and_b32_e32 v12, 0xffff0000, v15
	v_lshlrev_b32_e32 v11, 16, v15
	v_mul_f32_e32 v12, v12, v12
	v_fmac_f32_e32 v12, v11, v11
	v_add_f32_e32 v2, v12, v2
	ds_bpermute_b32 v11, v1, v2
	s_waitcnt lgkmcnt(0)
	v_add_f32_e32 v2, v2, v11
	ds_bpermute_b32 v11, v6, v2
	s_waitcnt lgkmcnt(0)
	v_add_f32_e32 v11, v2, v11
	ds_bpermute_b32 v12, v9, v11
	s_and_saveexec_b64 s[12:13], vcc
	s_cbranch_execz .LBB0_1191
	v_lshlrev_b32_e32 v2, 6, v10
	v_lshl_add_u64 v[14:15], s[10:11], 0, v[2:3]
	s_waitcnt lgkmcnt(0)
	v_add_f32_e32 v2, v11, v12
	flat_store_dword v[14:15], v2 sc1
.LBB0_1191:
	s_or_b64 exec, exec, s[12:13]
	v_or_b32_e32 v10, 16, v7
	v_lshl_add_u32 v2, v10, 7, v8
	s_waitcnt lgkmcnt(0)
	ds_read_b128 v[12:15], v2
	v_lshlrev_b32_e32 v2, 11, v10
	v_lshl_add_u64 v[16:17], v[4:5], 0, v[2:3]
	s_waitcnt lgkmcnt(0)
	v_and_b32_e32 v11, 0xffff0000, v12
	global_store_dwordx4 v[16:17], v[12:15], off sc1
	v_lshlrev_b32_e32 v2, 16, v12
	v_mul_f32_e32 v11, v11, v11
	v_and_b32_e32 v12, 0xffff0000, v13
	v_fmac_f32_e32 v11, v2, v2
	v_lshlrev_b32_e32 v2, 16, v13
	v_mul_f32_e32 v12, v12, v12
	v_fmac_f32_e32 v12, v2, v2
	v_add_f32_e32 v2, v11, v12
	v_and_b32_e32 v12, 0xffff0000, v14
	v_lshlrev_b32_e32 v11, 16, v14
	v_mul_f32_e32 v12, v12, v12
	v_fmac_f32_e32 v12, v11, v11
	v_add_f32_e32 v2, v12, v2
	v_and_b32_e32 v12, 0xffff0000, v15
	v_lshlrev_b32_e32 v11, 16, v15
	v_mul_f32_e32 v12, v12, v12
	v_fmac_f32_e32 v12, v11, v11
	v_add_f32_e32 v2, v12, v2
	ds_bpermute_b32 v11, v1, v2
	s_waitcnt lgkmcnt(0)
	v_add_f32_e32 v2, v2, v11
	ds_bpermute_b32 v11, v6, v2
	s_waitcnt lgkmcnt(0)
	v_add_f32_e32 v11, v2, v11
	ds_bpermute_b32 v12, v9, v11
	s_and_saveexec_b64 s[12:13], vcc
	s_cbranch_execz .LBB0_1193
	v_lshlrev_b32_e32 v2, 6, v10
	v_lshl_add_u64 v[14:15], s[10:11], 0, v[2:3]
	s_waitcnt lgkmcnt(0)
	v_add_f32_e32 v2, v11, v12
	flat_store_dword v[14:15], v2 sc1
.LBB0_1193:
	s_or_b64 exec, exec, s[12:13]
	v_or_b32_e32 v7, 24, v7
	v_lshl_add_u32 v2, v7, 7, v8
	s_waitcnt lgkmcnt(0)
	ds_read_b128 v[10:13], v2
	v_lshlrev_b32_e32 v2, 11, v7
	v_lshl_add_u64 v[4:5], v[4:5], 0, v[2:3]
	s_waitcnt lgkmcnt(0)
	global_store_dwordx4 v[4:5], v[10:13], off sc1
	v_and_b32_e32 v4, 0xffff0000, v10
	v_lshlrev_b32_e32 v2, 16, v10
	v_mul_f32_e32 v4, v4, v4
	v_and_b32_e32 v5, 0xffff0000, v11
	v_fmac_f32_e32 v4, v2, v2
	v_lshlrev_b32_e32 v2, 16, v11
	v_mul_f32_e32 v5, v5, v5
	v_fmac_f32_e32 v5, v2, v2
	v_add_f32_e32 v2, v4, v5
	v_and_b32_e32 v5, 0xffff0000, v12
	v_lshlrev_b32_e32 v4, 16, v12
	v_mul_f32_e32 v5, v5, v5
	v_fmac_f32_e32 v5, v4, v4
	v_add_f32_e32 v2, v5, v2
	v_and_b32_e32 v5, 0xffff0000, v13
	v_lshlrev_b32_e32 v4, 16, v13
	v_mul_f32_e32 v5, v5, v5
	v_fmac_f32_e32 v5, v4, v4
	v_add_f32_e32 v2, v5, v2
	ds_bpermute_b32 v1, v1, v2
	s_waitcnt lgkmcnt(0)
	v_add_f32_e32 v1, v2, v1
	ds_bpermute_b32 v2, v6, v1
	s_waitcnt lgkmcnt(0)
	v_add_f32_e32 v1, v1, v2
	ds_bpermute_b32 v4, v9, v1
	s_and_saveexec_b64 s[12:13], vcc
	s_cbranch_execz .LBB0_1131
	v_lshlrev_b32_e32 v2, 6, v7
	v_lshl_add_u64 v[6:7], s[10:11], 0, v[2:3]
	s_waitcnt lgkmcnt(0)
	v_add_f32_e32 v1, v1, v4
	flat_store_dword v[6:7], v1 sc1
	s_branch .LBB0_1131
